# layer-0 gather: same treatment as the final-layer one (ids one step ahead, remaining u-row loads issued mid-step, single deferred wait before the gelu)
# speedup vs baseline: 1.0201x; 1.0063x over previous
.Lgprio_l:
	v_add_u32_e32 v0, s6, v0
	v_cmp_gt_i32_e32 vcc, s87, v0
	s_and_saveexec_b64 s[6:7], vcc
	s_mov_b32 s12, 0x800000
	s_cbranch_execz .LBB0_772
	v_ashrrev_i32_e32 v1, 31, v0
	v_and_b32_e32 v2, 15, v3
	v_lshlrev_b64 v[4:5], 9, v[0:1]
	v_lshl_add_u64 v[8:9], s[94:95], 0, v[4:5]
	v_lshlrev_b32_e32 v144, 2, v2
	v_lshl_add_u64 v[8:9], v[8:9], 0, v[144:145]
	global_load_dword v96, v[8:9], off
	global_load_dword v122, v[8:9], off offset:64
	v_and_b32_e32 v6, 63, v3
	v_readlane_b32 s10, v253, 27
	v_lshlrev_b32_e32 v144, 3, v6
	v_readlane_b32 s11, v253, 28
	s_load_dwordx2 s[8:9], s[8:9], 0x10
	v_and_b32_e32 v1, 32, v3
	v_lshl_add_u64 v[16:17], s[10:11], 0, v[144:145]
	v_readlane_b32 s10, v253, 29
	v_readlane_b32 s11, v253, 30
	v_cmp_eq_u32_e64 s[40:41], 0, v1
	v_and_b32_e32 v1, 16, v3
	v_lshl_add_u64 v[18:19], s[10:11], 0, v[144:145]
	v_lshlrev_b32_e32 v144, 5, v6
	v_and_b32_e32 v97, 60, v3
	v_cmp_eq_u32_e64 s[42:43], 0, v1
	v_and_b32_e32 v1, 8, v3
	v_cmp_eq_u32_e64 s[44:45], 0, v1
	v_and_b32_e32 v1, 4, v3
	v_or_b32_e32 v4, v4, v97
	v_cmp_eq_u32_e64 s[46:47], 0, v1
	s_waitcnt vmcnt(0)
	v_readlane_b32 s10, v96, 0
	s_ashr_i32 s11, s10, 31
	s_lshl_b64 s[10:11], s[10:11], 9
	v_lshl_add_u64 v[8:9], v[16:17], 0, s[10:11]
	global_load_dwordx2 v[20:21], v[8:9], off
	v_lshl_add_u64 v[8:9], v[18:19], 0, s[10:11]
	v_readlane_b32 s10, v96, 1
	s_ashr_i32 s11, s10, 31
	s_lshl_b64 s[10:11], s[10:11], 9
	global_load_dwordx2 v[92:93], v[8:9], off
	v_lshl_add_u64 v[8:9], v[16:17], 0, s[10:11]
	global_load_dwordx2 v[22:23], v[8:9], off
	v_lshl_add_u64 v[8:9], v[18:19], 0, s[10:11]
	v_readlane_b32 s10, v96, 2
	s_ashr_i32 s11, s10, 31
	s_lshl_b64 s[10:11], s[10:11], 9
	global_load_dwordx2 v[90:91], v[8:9], off
	v_lshl_add_u64 v[8:9], v[16:17], 0, s[10:11]
	global_load_dwordx2 v[24:25], v[8:9], off
	v_lshl_add_u64 v[8:9], v[18:19], 0, s[10:11]
	v_readlane_b32 s10, v96, 3
	s_ashr_i32 s11, s10, 31
	s_lshl_b64 s[10:11], s[10:11], 9
	global_load_dwordx2 v[88:89], v[8:9], off
	v_lshl_add_u64 v[8:9], v[16:17], 0, s[10:11]
	global_load_dwordx2 v[26:27], v[8:9], off
	v_lshl_add_u64 v[8:9], v[18:19], 0, s[10:11]
	v_readlane_b32 s10, v96, 4
	s_ashr_i32 s11, s10, 31
	s_lshl_b64 s[10:11], s[10:11], 9
	global_load_dwordx2 v[86:87], v[8:9], off
	v_lshl_add_u64 v[8:9], v[16:17], 0, s[10:11]
	global_load_dwordx2 v[28:29], v[8:9], off
	v_lshl_add_u64 v[8:9], v[18:19], 0, s[10:11]
	v_readlane_b32 s10, v96, 5
	s_ashr_i32 s11, s10, 31
	s_lshl_b64 s[10:11], s[10:11], 9
	global_load_dwordx2 v[84:85], v[8:9], off
	v_lshl_add_u64 v[8:9], v[16:17], 0, s[10:11]
	global_load_dwordx2 v[30:31], v[8:9], off
	v_lshl_add_u64 v[8:9], v[18:19], 0, s[10:11]
	v_readlane_b32 s10, v96, 6
	s_ashr_i32 s11, s10, 31
	s_lshl_b64 s[10:11], s[10:11], 9
	global_load_dwordx2 v[82:83], v[8:9], off
	v_lshl_add_u64 v[8:9], v[16:17], 0, s[10:11]
	global_load_dwordx2 v[32:33], v[8:9], off
	v_lshl_add_u64 v[8:9], v[18:19], 0, s[10:11]
	v_readlane_b32 s10, v96, 7
	s_ashr_i32 s11, s10, 31
	s_lshl_b64 s[10:11], s[10:11], 9
	global_load_dwordx2 v[80:81], v[8:9], off
	v_lshl_add_u64 v[8:9], v[16:17], 0, s[10:11]
	global_load_dwordx2 v[34:35], v[8:9], off
	v_lshl_add_u64 v[8:9], v[18:19], 0, s[10:11]
	v_readlane_b32 s10, v96, 8
	s_ashr_i32 s11, s10, 31
	s_lshl_b64 s[10:11], s[10:11], 9
	global_load_dwordx2 v[78:79], v[8:9], off
	v_lshl_add_u64 v[8:9], v[16:17], 0, s[10:11]
	global_load_dwordx2 v[36:37], v[8:9], off
	v_lshl_add_u64 v[8:9], v[18:19], 0, s[10:11]
	v_readlane_b32 s10, v96, 9
	s_ashr_i32 s11, s10, 31
	s_lshl_b64 s[10:11], s[10:11], 9
	global_load_dwordx2 v[76:77], v[8:9], off
	v_lshl_add_u64 v[8:9], v[16:17], 0, s[10:11]
	global_load_dwordx2 v[38:39], v[8:9], off
	v_lshl_add_u64 v[8:9], v[18:19], 0, s[10:11]
	v_readlane_b32 s10, v96, 10
	s_ashr_i32 s11, s10, 31
	s_lshl_b64 s[10:11], s[10:11], 9
	global_load_dwordx2 v[70:71], v[8:9], off
	v_lshl_add_u64 v[8:9], v[16:17], 0, s[10:11]
	global_load_dwordx2 v[40:41], v[8:9], off
	v_lshl_add_u64 v[8:9], v[18:19], 0, s[10:11]
	v_readlane_b32 s10, v96, 11
	s_ashr_i32 s11, s10, 31
	s_lshl_b64 s[10:11], s[10:11], 9
	global_load_dwordx2 v[66:67], v[8:9], off
	v_lshl_add_u64 v[8:9], v[16:17], 0, s[10:11]
	global_load_dwordx2 v[60:61], v[8:9], off
	v_lshl_add_u64 v[8:9], v[18:19], 0, s[10:11]
	v_readlane_b32 s10, v96, 12
	s_ashr_i32 s11, s10, 31
	s_lshl_b64 s[10:11], s[10:11], 9
	global_load_dwordx2 v[72:73], v[8:9], off
	v_lshl_add_u64 v[8:9], v[16:17], 0, s[10:11]
	global_load_dwordx2 v[58:59], v[8:9], off
	v_lshl_add_u64 v[8:9], v[18:19], 0, s[10:11]
	v_readlane_b32 s10, v96, 13
	s_ashr_i32 s11, s10, 31
	s_lshl_b64 s[10:11], s[10:11], 9
	global_load_dwordx2 v[68:69], v[8:9], off
	v_lshl_add_u64 v[8:9], v[16:17], 0, s[10:11]
	global_load_dwordx2 v[56:57], v[8:9], off
	v_lshl_add_u64 v[8:9], v[18:19], 0, s[10:11]
	v_readlane_b32 s10, v96, 14
	s_ashr_i32 s11, s10, 31
	s_lshl_b64 s[10:11], s[10:11], 9
	global_load_dwordx2 v[64:65], v[8:9], off
	v_lshl_add_u64 v[8:9], v[16:17], 0, s[10:11]
	global_load_dwordx2 v[54:55], v[8:9], off
	v_lshl_add_u64 v[8:9], v[18:19], 0, s[10:11]
	v_readlane_b32 s10, v96, 15
	s_ashr_i32 s11, s10, 31
	s_lshl_b64 s[10:11], s[10:11], 9
	global_load_dwordx2 v[62:63], v[8:9], off
	v_lshl_add_u64 v[8:9], v[16:17], 0, s[10:11]
	global_load_dwordx2 v[52:53], v[8:9], off
	v_lshl_add_u64 v[8:9], v[18:19], 0, s[10:11]
	global_load_dwordx2 v[50:51], v[8:9], off
	v_readlane_b32 s10, v253, 15
	v_readlane_b32 s11, v253, 16
	s_nop 1
	v_lshl_add_u64 v[42:43], s[10:11], 0, v[144:145]
	v_lshlrev_b32_e32 v144, 6, v6
	s_waitcnt lgkmcnt(0)
	v_lshl_add_u64 v[6:7], s[8:9], 0, v[144:145]
	s_mov_b64 s[8:9], 0x1000
	v_readlane_b32 s10, v253, 13
	v_lshl_add_u64 v[46:47], v[6:7], 0, s[8:9]
	v_readlane_b32 s8, v253, 23
	v_readlane_b32 s11, v253, 14
	v_readlane_b32 s9, v253, 24
	s_nop 0
	v_lshl_add_u64 v[44:45], s[10:11], 0, v[144:145]
	v_lshl_add_u64 v[48:49], s[8:9], 0, v[4:5]
	s_mov_b64 s[8:9], 0
	v_lshlrev_b32_e32 v144, 2, v2
	v_readfirstlane_b32 s62, v16
	v_readfirstlane_b32 s63, v17
	v_readfirstlane_b32 s64, v18
	v_readfirstlane_b32 s65, v19
	v_and_b32_e32 v121, 63, v175
	v_lshlrev_b32_e32 v121, 3, v121

.LBB0_770:
	s_cmpk_ge_i32 s56, 0x70
	s_cselect_b64 s[10:11], -1, 0
	ds_bpermute_b32 v6, v97, v96
	s_and_b64 vcc, s[10:11], s[48:49]
	v_cndmask_b32_e32 v94, v0, v98, vcc
	v_ashrrev_i32_e32 v95, 31, v94
	s_add_i32 s10, s56, 16
	s_and_b32 s10, s10, 0x70
	v_lshlrev_b64 v[94:95], 9, v[94:95]
	v_lshl_add_u64 v[94:95], s[94:95], 0, v[94:95]
	s_lshl_b32 s36, s10, 2
	s_waitcnt lgkmcnt(0)
	s_waitcnt vmcnt(32)
	v_mov_b32_e32 v96, v122
	v_ashrrev_i32_e32 v7, 31, v6
	v_lshl_add_u64 v[94:95], v[94:95], 0, s[36:37]
	v_lshl_add_u64 v[6:7], v[6:7], 3, s[88:89]
	v_lshl_add_u64 v[94:95], v[94:95], 0, v[144:145]
	global_load_dwordx2 v[6:7], v[6:7], off
	s_nop 0
	global_load_dword v8, v[4:5], off
	global_load_dword v122, v[94:95], off
	s_waitcnt vmcnt(19)
	v_dot8_i32_i4 v9, v20, v1, 0
	v_dot8_i32_i4 v94, v20, v10, 0
	v_dot8_i32_i4 v9, v21, v11, v9
	v_dot8_i32_i4 v94, v21, v12, v94
	v_dot8_i32_i4 v20, v22, v1, 0
	v_dot8_i32_i4 v21, v22, v10, 0
	v_dot8_i32_i4 v20, v23, v11, v20
	v_dot8_i32_i4 v21, v23, v12, v21
	v_lshl_add_u32 v9, v9, 4, v94
	s_add_i32 s56, s56, 16
	s_nop 0
	v_lshl_add_u32 v94, v20, 4, v21
	s_waitcnt vmcnt(19)
	v_dot8_i32_i4 v20, v24, v1, 0
	v_dot8_i32_i4 v21, v24, v10, 0
	v_dot8_i32_i4 v20, v25, v11, v20
	v_dot8_i32_i4 v21, v25, v12, v21
	v_lshl_add_u64 v[4:5], v[4:5], 0, 64
	s_nop 1
	v_lshl_add_u32 v95, v20, 4, v21
	v_dot8_i32_i4 v20, v26, v1, 0
	v_dot8_i32_i4 v21, v26, v10, 0
	v_dot8_i32_i4 v20, v27, v11, v20
	v_dot8_i32_i4 v21, v27, v12, v21
	v_readlane_b32 s10, v96, 0
	s_ashr_i32 s11, s10, 31
	v_readlane_b32 s12, v96, 1
	v_lshl_add_u32 v106, v20, 4, v21
	v_dot8_i32_i4 v20, v28, v1, 0
	v_dot8_i32_i4 v21, v28, v10, 0
	v_dot8_i32_i4 v20, v29, v11, v20
	v_dot8_i32_i4 v21, v29, v12, v21
	s_lshl_b64 s[10:11], s[10:11], 9
	s_ashr_i32 s13, s12, 31
	v_readlane_b32 s14, v96, 2
	v_lshl_add_u32 v107, v20, 4, v21
	v_dot8_i32_i4 v20, v30, v1, 0
	v_dot8_i32_i4 v21, v30, v10, 0
	v_dot8_i32_i4 v20, v31, v11, v20
	v_dot8_i32_i4 v21, v31, v12, v21
	s_lshl_b64 s[12:13], s[12:13], 9
	s_ashr_i32 s15, s14, 31
	v_readlane_b32 s16, v96, 3
	v_lshl_add_u32 v108, v20, 4, v21
	v_dot8_i32_i4 v20, v32, v1, 0
	v_dot8_i32_i4 v21, v32, v10, 0
	v_dot8_i32_i4 v20, v33, v11, v20
	v_dot8_i32_i4 v21, v33, v12, v21
	s_lshl_b64 s[14:15], s[14:15], 9
	s_ashr_i32 s17, s16, 31
	s_nop 0
	v_lshl_add_u32 v109, v20, 4, v21
	v_dot8_i32_i4 v20, v34, v1, 0
	v_dot8_i32_i4 v21, v34, v10, 0
	v_dot8_i32_i4 v20, v35, v11, v20
	v_dot8_i32_i4 v21, v35, v12, v21
	v_readlane_b32 s18, v96, 4
	s_add_u32 s66, s12, s62
	s_addc_u32 s67, s13, s63
	global_load_dwordx2 v[22:23], v121, s[66:67]
	v_lshl_add_u32 v110, v20, 4, v21
	v_dot8_i32_i4 v20, v36, v1, 0
	v_dot8_i32_i4 v21, v36, v10, 0
	v_dot8_i32_i4 v20, v37, v11, v20
	v_dot8_i32_i4 v21, v37, v12, v21
	s_lshl_b64 s[16:17], s[16:17], 9
	s_ashr_i32 s19, s18, 31
	v_readlane_b32 s20, v96, 5
	v_lshl_add_u32 v111, v20, 4, v21
	v_dot8_i32_i4 v20, v38, v1, 0
	v_dot8_i32_i4 v21, v38, v10, 0
	v_dot8_i32_i4 v20, v39, v11, v20
	v_dot8_i32_i4 v21, v39, v12, v21
	s_setprio 2
	v_permlane32_swap_b32 v9, v111
	s_nop 1
	v_lshl_add_u32 v112, v20, 4, v21
	v_dot8_i32_i4 v20, v40, v1, 0
	v_dot8_i32_i4 v21, v40, v10, 0
	v_dot8_i32_i4 v20, v41, v11, v20
	v_dot8_i32_i4 v21, v41, v12, v21
	s_waitcnt lgkmcnt(0)
	v_add_u32_e32 v9, v9, v111
	v_permlane32_swap_b32 v94, v112
	v_lshl_add_u32 v113, v20, 4, v21
	v_dot8_i32_i4 v20, v60, v1, 0
	v_dot8_i32_i4 v21, v60, v10, 0
	v_dot8_i32_i4 v20, v61, v11, v20
	v_dot8_i32_i4 v21, v61, v12, v21
	s_waitcnt lgkmcnt(0)
	v_add_u32_e32 v94, v94, v112
	v_permlane32_swap_b32 v95, v113
	v_lshl_add_u32 v114, v20, 4, v21
	v_dot8_i32_i4 v20, v58, v1, 0
	v_dot8_i32_i4 v21, v58, v10, 0
	v_dot8_i32_i4 v20, v59, v11, v20
	v_dot8_i32_i4 v21, v59, v12, v21
	s_waitcnt lgkmcnt(0)
	v_add_u32_e32 v95, v95, v113
	v_permlane32_swap_b32 v106, v114
	v_lshl_add_u32 v115, v20, 4, v21
	v_dot8_i32_i4 v20, v56, v1, 0
	v_dot8_i32_i4 v21, v56, v10, 0
	v_dot8_i32_i4 v20, v57, v11, v20
	v_dot8_i32_i4 v21, v57, v12, v21
	s_waitcnt lgkmcnt(0)
	v_add_u32_e32 v106, v106, v114
	v_permlane32_swap_b32 v107, v115
	v_lshl_add_u32 v116, v20, 4, v21
	v_dot8_i32_i4 v20, v54, v1, 0
	v_dot8_i32_i4 v21, v54, v10, 0
	v_dot8_i32_i4 v20, v55, v11, v20
	v_dot8_i32_i4 v21, v55, v12, v21
	s_waitcnt lgkmcnt(0)
	v_add_u32_e32 v107, v107, v115
	v_permlane32_swap_b32 v108, v116
	v_lshl_add_u32 v117, v20, 4, v21
	v_dot8_i32_i4 v20, v52, v1, 0
	v_dot8_i32_i4 v21, v52, v10, 0
	v_dot8_i32_i4 v20, v53, v11, v20
	v_dot8_i32_i4 v21, v53, v12, v21
	s_waitcnt lgkmcnt(0)
	v_add_u32_e32 v108, v108, v116
	v_permlane32_swap_b32 v109, v117
	v_lshl_add_u32 v118, v20, 4, v21
	s_waitcnt lgkmcnt(0)
	v_add_u32_e32 v109, v109, v117
	v_permlane32_swap_b32 v110, v118
	s_add_u32 s66, s10, s62
	s_addc_u32 s67, s11, s63
	global_load_dwordx2 v[20:21], v121, s[66:67]
	s_add_u32 s66, s14, s62
	s_addc_u32 s67, s15, s63
	global_load_dwordx2 v[24:25], v121, s[66:67]
	s_waitcnt lgkmcnt(0)
	v_add_u32_e32 v110, v110, v118
	v_permlane16_swap_b32 v9, v107
	s_lshl_b64 s[18:19], s[18:19], 9
	s_ashr_i32 s21, s20, 31
	v_readlane_b32 s22, v96, 6
	s_add_u32 s66, s16, s62
	s_addc_u32 s67, s17, s63
	global_load_dwordx2 v[26:27], v121, s[66:67]
	s_waitcnt lgkmcnt(0)
	v_add_u32_e32 v9, v9, v107
	v_permlane16_swap_b32 v94, v108
	s_lshl_b64 s[20:21], s[20:21], 9
	s_ashr_i32 s23, s22, 31
	s_waitcnt lgkmcnt(0)
	v_add_u32_e32 v94, v94, v108
	v_permlane16_swap_b32 v95, v109
	v_readlane_b32 s24, v96, 7
	s_add_u32 s66, s18, s62
	s_addc_u32 s67, s19, s63
	global_load_dwordx2 v[28:29], v121, s[66:67]
	s_waitcnt lgkmcnt(0)
	v_add_u32_e32 v95, v95, v109
	v_permlane16_swap_b32 v106, v110
	s_lshl_b64 s[22:23], s[22:23], 9
	s_ashr_i32 s25, s24, 31
	v_readlane_b32 s26, v96, 8
	s_waitcnt lgkmcnt(0)
	v_add_u32_e32 v106, v106, v110
	v_cndmask_b32_e64 v107, v9, v95, s[44:45]
	v_cndmask_b32_e64 v9, v95, v9, s[44:45]
	s_nop 0
	s_add_u32 s66, s20, s62
	s_addc_u32 s67, s21, s63
	global_load_dwordx2 v[30:31], v121, s[66:67]
	s_lshl_b64 s[24:25], s[24:25], 9
	s_ashr_i32 s27, s26, 31
	s_waitcnt lgkmcnt(0)
	v_add_u32_dpp v9, v107, v9 row_ror:8 row_mask:0xf bank_mask:0xf
	v_cndmask_b32_e64 v95, v94, v106, s[44:45]
	s_nop 1
	v_cndmask_b32_e64 v94, v106, v94, s[44:45]
	v_readlane_b32 s28, v96, 9
	s_add_u32 s66, s22, s62
	s_addc_u32 s67, s23, s63
	global_load_dwordx2 v[32:33], v121, s[66:67]
	s_waitcnt lgkmcnt(0)
	v_add_u32_dpp v94, v95, v94 row_ror:8 row_mask:0xf bank_mask:0xf
	v_cndmask_b32_e64 v95, v9, v94, s[46:47]
	v_cndmask_b32_e64 v9, v94, v9, s[46:47]
	s_nop 0
	v_mov_b32_dpp v94, v95 row_half_mirror row_mask:0xf bank_mask:0xf
	s_nop 1
	s_lshl_b64 s[26:27], s[26:27], 9
	s_ashr_i32 s29, s28, 31
	v_readlane_b32 s30, v96, 10
	s_add_u32 s66, s24, s62
	s_addc_u32 s67, s25, s63
	global_load_dwordx2 v[34:35], v121, s[66:67]
	s_waitcnt lgkmcnt(0)
	v_add_u32_dpp v9, v94, v9 quad_perm:[3,2,1,0] row_mask:0xf bank_mask:0xf
	s_nop 1
	s_lshl_b64 s[28:29], s[28:29], 9
	s_ashr_i32 s31, s30, 31
	v_readlane_b32 s34, v96, 11
	s_waitcnt lgkmcnt(0)
	v_add_u32_dpp v9, v9, v9 quad_perm:[2,3,0,1] row_mask:0xf bank_mask:0xf
	s_nop 1
	s_add_u32 s66, s26, s62
	s_addc_u32 s67, s27, s63
	global_load_dwordx2 v[36:37], v121, s[66:67]
	s_lshl_b64 s[30:31], s[30:31], 9
	s_ashr_i32 s35, s34, 31
	s_waitcnt lgkmcnt(0)
	v_add_u32_dpp v9, v9, v9 quad_perm:[1,0,3,2] row_mask:0xf bank_mask:0xf
	s_waitcnt vmcnt(10)
	v_mul_f32_e32 v7, v13, v7
	v_cvt_f32_i32_e32 v9, v9
	v_add_f32_e32 v9, v14, v9
	v_mul_f32_e32 v7, v7, v9
	v_mul_f32_e32 v9, 0x3d372713, v7
	v_mul_f32_e32 v9, v7, v9
	v_fma_f32 v9, v7, v9, v7
	v_mul_f32_e32 v9, 0x3fcc422a, v9
	v_mul_f32_e32 v9, 0xbfb8aa3b, v9
	v_exp_f32_e32 v9, v9
	v_readlane_b32 s38, v96, 12
	s_add_u32 s66, s28, s62
	s_addc_u32 s67, s29, s63
	global_load_dwordx2 v[38:39], v121, s[66:67]
	v_add_f32_e32 v9, 1.0, v9
	v_rcp_f32_e32 v9, v9
	s_lshl_b64 s[34:35], s[34:35], 9
	s_ashr_i32 s39, s38, 31
	s_lshl_b64 s[38:39], s[38:39], 9
	v_readlane_b32 s50, v96, 13
	v_readlane_b32 s52, v96, 14
	v_readlane_b32 s54, v96, 15
	s_ashr_i32 s51, s50, 31
	s_ashr_i32 s53, s52, 31
	s_ashr_i32 s55, s54, 31
	s_lshl_b64 s[50:51], s[50:51], 9
	s_lshl_b64 s[52:53], s[52:53], 9
	s_lshl_b64 s[54:55], s[54:55], 9
	s_add_u32 s66, s30, s62
	s_addc_u32 s67, s31, s63
	global_load_dwordx2 v[40:41], v121, s[66:67]
	s_add_u32 s66, s34, s62
	s_addc_u32 s67, s35, s63
	global_load_dwordx2 v[60:61], v121, s[66:67]
	s_add_u32 s66, s38, s62
	s_addc_u32 s67, s39, s63
	global_load_dwordx2 v[58:59], v121, s[66:67]
	s_add_u32 s66, s50, s62
	s_addc_u32 s67, s51, s63
	global_load_dwordx2 v[56:57], v121, s[66:67]
	s_add_u32 s66, s52, s62
	s_addc_u32 s67, s53, s63
	global_load_dwordx2 v[54:55], v121, s[66:67]
	s_add_u32 s66, s54, s62
	s_addc_u32 s67, s55, s63
	global_load_dwordx2 v[52:53], v121, s[66:67]
	v_pk_mul_f32 v[6:7], v[6:7], v[8:9]
	v_alignbit_b32 v224, v92, v92, 4
	v_pk_mul_f32 v[6:7], v[6:7], v[6:7] op_sel:[0,1] op_sel_hi:[1,0]
	v_cvt_f16_f32_e32 v120, v6
	s_setprio 0
	v_and_b32_e32 v8, 0x7070707, v92
	v_readlane_b32 s36, v120, 0
	v_and_b32_e32 v9, 0x7070707, v224
	v_perm_b32 v8, s2, v205, v8
	v_perm_b32 v9, s2, v205, v9
	v_and_or_b32 v8, v92, s4, v8
	v_and_or_b32 v9, v224, s4, v9
	v_perm_b32 v92, v9, v8, s5
	v_perm_b32 v94, v9, v8, s33
	v_perm_b32 v95, v9, v8, s0
	v_perm_b32 v8, v9, v8, s1
	v_pk_fma_f16 v8, v8, s36, v102 op_sel_hi:[1,0,1]
	v_alignbit_b32 v225, v93, v93, 4
	v_pk_fma_f16 v9, v92, s36, v105 op_sel_hi:[1,0,1]
	v_pk_fma_f16 v92, v94, s36, v104 op_sel_hi:[1,0,1]
	v_pk_fma_f16 v94, v95, s36, v103 op_sel_hi:[1,0,1]
	v_and_b32_e32 v95, 0x7070707, v93
	v_and_b32_e32 v102, 0x7070707, v225
	v_perm_b32 v95, s2, v205, v95
	v_perm_b32 v102, s2, v205, v102
	v_and_or_b32 v95, v93, s4, v95
	v_and_or_b32 v93, v225, s4, v102
	v_perm_b32 v102, v93, v95, s5
	v_perm_b32 v103, v93, v95, s33
	v_perm_b32 v104, v93, v95, s0
	v_perm_b32 v93, v93, v95, s1
	v_pk_fma_f16 v95, v102, s36, v101 op_sel_hi:[1,0,1]
	v_readlane_b32 s59, v120, 4
	v_alignbit_b32 v224, v90, v90, 4
	v_pk_fma_f16 v100, v103, s36, v100 op_sel_hi:[1,0,1]
	v_pk_fma_f16 v99, v104, s36, v99 op_sel_hi:[1,0,1]
	v_pk_fma_f16 v7, v93, s36, v15 op_sel_hi:[1,0,1]
	v_and_b32_e32 v93, 0x7070707, v90
	v_and_b32_e32 v101, 0x7070707, v224
	v_perm_b32 v93, s2, v205, v93
	v_perm_b32 v101, s2, v205, v101
	v_and_or_b32 v93, v90, s4, v93
	v_and_or_b32 v90, v224, s4, v101
	v_perm_b32 v103, v90, v93, s0
	v_perm_b32 v101, v90, v93, s5
	v_perm_b32 v102, v90, v93, s33
	v_perm_b32 v90, v90, v93, s1
	v_pk_fma_f16 v93, v103, s59, v94 op_sel_hi:[1,0,1]
	v_alignbit_b32 v225, v91, v91, 4
	v_pk_fma_f16 v8, v90, s59, v8 op_sel_hi:[1,0,1]
	v_and_b32_e32 v90, 0x7070707, v91
	v_and_b32_e32 v94, 0x7070707, v225
	v_pk_fma_f16 v9, v101, s59, v9 op_sel_hi:[1,0,1]
	v_perm_b32 v90, s2, v205, v90
	v_perm_b32 v94, s2, v205, v94
	v_and_or_b32 v90, v91, s4, v90
	v_and_or_b32 v91, v225, s4, v94
	v_pk_fma_f16 v92, v102, s59, v92 op_sel_hi:[1,0,1]
	v_perm_b32 v94, v91, v90, s5
	v_perm_b32 v102, v91, v90, s0
	v_perm_b32 v101, v91, v90, s33
	v_perm_b32 v90, v91, v90, s1
	v_pk_fma_f16 v91, v94, s59, v95 op_sel_hi:[1,0,1]
	v_pk_fma_f16 v95, v102, s59, v99 op_sel_hi:[1,0,1]
	v_readlane_b32 s60, v120, 8
	v_alignbit_b32 v224, v88, v88, 4
	v_pk_fma_f16 v94, v101, s59, v100 op_sel_hi:[1,0,1]
	v_pk_fma_f16 v7, v90, s59, v7 op_sel_hi:[1,0,1]
	v_and_b32_e32 v90, 0x7070707, v88
	v_and_b32_e32 v99, 0x7070707, v224
	v_perm_b32 v90, s2, v205, v90
	v_perm_b32 v99, s2, v205, v99
	v_and_or_b32 v90, v88, s4, v90
	v_and_or_b32 v88, v224, s4, v99
	v_perm_b32 v100, v88, v90, s33
	v_perm_b32 v101, v88, v90, s0
	v_perm_b32 v99, v88, v90, s5
	v_perm_b32 v88, v88, v90, s1
	v_pk_fma_f16 v90, v100, s60, v92 op_sel_hi:[1,0,1]
	v_pk_fma_f16 v92, v101, s60, v93 op_sel_hi:[1,0,1]
	v_alignbit_b32 v225, v89, v89, 4
	v_pk_fma_f16 v8, v88, s60, v8 op_sel_hi:[1,0,1]
	v_and_b32_e32 v88, 0x7070707, v89
	v_and_b32_e32 v93, 0x7070707, v225
	v_pk_fma_f16 v9, v99, s60, v9 op_sel_hi:[1,0,1]
	v_perm_b32 v88, s2, v205, v88
	v_perm_b32 v93, s2, v205, v93
	v_and_or_b32 v88, v89, s4, v88
	v_and_or_b32 v89, v225, s4, v93
	v_perm_b32 v93, v89, v88, s5
	v_perm_b32 v99, v89, v88, s33
	v_perm_b32 v100, v89, v88, s0
	v_perm_b32 v88, v89, v88, s1
	v_pk_fma_f16 v89, v93, s60, v91 op_sel_hi:[1,0,1]
	v_pk_fma_f16 v91, v99, s60, v94 op_sel_hi:[1,0,1]
	v_readlane_b32 s36, v120, 12
	v_alignbit_b32 v224, v86, v86, 4
	v_pk_fma_f16 v93, v100, s60, v95 op_sel_hi:[1,0,1]
	v_pk_fma_f16 v7, v88, s60, v7 op_sel_hi:[1,0,1]
	v_and_b32_e32 v88, 0x7070707, v86
	v_and_b32_e32 v94, 0x7070707, v224
	v_perm_b32 v88, s2, v205, v88
	v_perm_b32 v94, s2, v205, v94
	v_and_or_b32 v88, v86, s4, v88
	v_and_or_b32 v86, v224, s4, v94
	v_perm_b32 v95, v86, v88, s33
	v_perm_b32 v99, v86, v88, s0
	v_perm_b32 v94, v86, v88, s5
	v_perm_b32 v86, v86, v88, s1
	v_pk_fma_f16 v88, v95, s36, v90 op_sel_hi:[1,0,1]
	v_pk_fma_f16 v90, v99, s36, v92 op_sel_hi:[1,0,1]
	v_alignbit_b32 v225, v87, v87, 4
	v_pk_fma_f16 v8, v86, s36, v8 op_sel_hi:[1,0,1]
	v_and_b32_e32 v86, 0x7070707, v87
	v_and_b32_e32 v92, 0x7070707, v225
	v_pk_fma_f16 v9, v94, s36, v9 op_sel_hi:[1,0,1]
	v_perm_b32 v86, s2, v205, v86
	v_perm_b32 v92, s2, v205, v92
	v_and_or_b32 v86, v87, s4, v86
	v_and_or_b32 v87, v225, s4, v92
	v_perm_b32 v92, v87, v86, s5
	v_perm_b32 v94, v87, v86, s33
	v_perm_b32 v95, v87, v86, s0
	v_perm_b32 v86, v87, v86, s1
	v_pk_fma_f16 v87, v92, s36, v89 op_sel_hi:[1,0,1]
	v_readlane_b32 s59, v120, 16
	v_alignbit_b32 v224, v84, v84, 4
	v_pk_fma_f16 v89, v94, s36, v91 op_sel_hi:[1,0,1]
	v_pk_fma_f16 v91, v95, s36, v93 op_sel_hi:[1,0,1]
	v_pk_fma_f16 v7, v86, s36, v7 op_sel_hi:[1,0,1]
	v_and_b32_e32 v86, 0x7070707, v84
	v_and_b32_e32 v92, 0x7070707, v224
	v_perm_b32 v86, s2, v205, v86
	v_perm_b32 v92, s2, v205, v92
	v_and_or_b32 v86, v84, s4, v86
	v_and_or_b32 v84, v224, s4, v92
	v_perm_b32 v93, v84, v86, s33
	v_perm_b32 v94, v84, v86, s0
	v_perm_b32 v92, v84, v86, s5
	v_perm_b32 v84, v84, v86, s1
	v_pk_fma_f16 v86, v93, s59, v88 op_sel_hi:[1,0,1]
	v_pk_fma_f16 v88, v94, s59, v90 op_sel_hi:[1,0,1]
	v_alignbit_b32 v225, v85, v85, 4
	v_pk_fma_f16 v8, v84, s59, v8 op_sel_hi:[1,0,1]
	v_and_b32_e32 v84, 0x7070707, v85
	v_and_b32_e32 v90, 0x7070707, v225
	v_pk_fma_f16 v9, v92, s59, v9 op_sel_hi:[1,0,1]
	v_perm_b32 v84, s2, v205, v84
	v_perm_b32 v90, s2, v205, v90
	v_and_or_b32 v84, v85, s4, v84
	v_and_or_b32 v85, v225, s4, v90
	v_perm_b32 v90, v85, v84, s5
	v_perm_b32 v92, v85, v84, s33
	v_perm_b32 v93, v85, v84, s0
	v_perm_b32 v84, v85, v84, s1
	v_pk_fma_f16 v85, v90, s59, v87 op_sel_hi:[1,0,1]
	v_readlane_b32 s60, v120, 20
	v_alignbit_b32 v224, v82, v82, 4
	v_pk_fma_f16 v87, v92, s59, v89 op_sel_hi:[1,0,1]
	v_pk_fma_f16 v89, v93, s59, v91 op_sel_hi:[1,0,1]
	v_pk_fma_f16 v7, v84, s59, v7 op_sel_hi:[1,0,1]
	v_and_b32_e32 v84, 0x7070707, v82
	v_and_b32_e32 v90, 0x7070707, v224
	v_perm_b32 v84, s2, v205, v84
	v_perm_b32 v90, s2, v205, v90
	v_and_or_b32 v84, v82, s4, v84
	v_and_or_b32 v82, v224, s4, v90
	v_perm_b32 v91, v82, v84, s33
	v_perm_b32 v92, v82, v84, s0
	v_perm_b32 v90, v82, v84, s5
	v_perm_b32 v82, v82, v84, s1
	v_pk_fma_f16 v84, v91, s60, v86 op_sel_hi:[1,0,1]
	v_pk_fma_f16 v86, v92, s60, v88 op_sel_hi:[1,0,1]
	v_alignbit_b32 v225, v83, v83, 4
	v_pk_fma_f16 v8, v82, s60, v8 op_sel_hi:[1,0,1]
	v_and_b32_e32 v82, 0x7070707, v83
	v_and_b32_e32 v88, 0x7070707, v225
	v_pk_fma_f16 v9, v90, s60, v9 op_sel_hi:[1,0,1]
	v_perm_b32 v82, s2, v205, v82
	v_perm_b32 v88, s2, v205, v88
	v_and_or_b32 v82, v83, s4, v82
	v_and_or_b32 v83, v225, s4, v88
	v_perm_b32 v88, v83, v82, s5
	v_perm_b32 v90, v83, v82, s33
	v_perm_b32 v91, v83, v82, s0
	v_perm_b32 v82, v83, v82, s1
	v_pk_fma_f16 v83, v88, s60, v85 op_sel_hi:[1,0,1]
	v_readlane_b32 s36, v120, 24
	v_alignbit_b32 v224, v80, v80, 4
	v_pk_fma_f16 v85, v90, s60, v87 op_sel_hi:[1,0,1]
	v_pk_fma_f16 v87, v91, s60, v89 op_sel_hi:[1,0,1]
	v_pk_fma_f16 v7, v82, s60, v7 op_sel_hi:[1,0,1]
	v_and_b32_e32 v82, 0x7070707, v80
	v_and_b32_e32 v88, 0x7070707, v224
	v_perm_b32 v82, s2, v205, v82
	v_perm_b32 v88, s2, v205, v88
	v_and_or_b32 v82, v80, s4, v82
	v_and_or_b32 v80, v224, s4, v88
	v_perm_b32 v89, v80, v82, s33
	v_perm_b32 v90, v80, v82, s0
	v_perm_b32 v88, v80, v82, s5
	v_perm_b32 v80, v80, v82, s1
	v_pk_fma_f16 v82, v89, s36, v84 op_sel_hi:[1,0,1]
	v_pk_fma_f16 v84, v90, s36, v86 op_sel_hi:[1,0,1]
	v_alignbit_b32 v225, v81, v81, 4
	v_pk_fma_f16 v8, v80, s36, v8 op_sel_hi:[1,0,1]
	v_and_b32_e32 v80, 0x7070707, v81
	v_and_b32_e32 v86, 0x7070707, v225
	v_pk_fma_f16 v9, v88, s36, v9 op_sel_hi:[1,0,1]
	v_perm_b32 v80, s2, v205, v80
	v_perm_b32 v86, s2, v205, v86
	v_and_or_b32 v80, v81, s4, v80
	v_and_or_b32 v81, v225, s4, v86
	v_perm_b32 v86, v81, v80, s5
	v_perm_b32 v88, v81, v80, s33
	v_perm_b32 v89, v81, v80, s0
	v_perm_b32 v80, v81, v80, s1
	v_pk_fma_f16 v81, v86, s36, v83 op_sel_hi:[1,0,1]
	v_readlane_b32 s59, v120, 28
	v_alignbit_b32 v224, v78, v78, 4
	v_pk_fma_f16 v83, v88, s36, v85 op_sel_hi:[1,0,1]
	v_pk_fma_f16 v85, v89, s36, v87 op_sel_hi:[1,0,1]
	v_pk_fma_f16 v7, v80, s36, v7 op_sel_hi:[1,0,1]
	v_and_b32_e32 v80, 0x7070707, v78
	v_and_b32_e32 v86, 0x7070707, v224
	v_perm_b32 v80, s2, v205, v80
	v_perm_b32 v86, s2, v205, v86
	v_and_or_b32 v80, v78, s4, v80
	v_and_or_b32 v78, v224, s4, v86
	v_perm_b32 v87, v78, v80, s33
	v_perm_b32 v88, v78, v80, s0
	v_perm_b32 v86, v78, v80, s5
	v_perm_b32 v78, v78, v80, s1
	v_pk_fma_f16 v80, v87, s59, v82 op_sel_hi:[1,0,1]
	v_pk_fma_f16 v82, v88, s59, v84 op_sel_hi:[1,0,1]
	v_alignbit_b32 v225, v79, v79, 4
	v_pk_fma_f16 v8, v78, s59, v8 op_sel_hi:[1,0,1]
	v_and_b32_e32 v78, 0x7070707, v79
	v_and_b32_e32 v84, 0x7070707, v225
	v_pk_fma_f16 v9, v86, s59, v9 op_sel_hi:[1,0,1]
	v_perm_b32 v78, s2, v205, v78
	v_perm_b32 v84, s2, v205, v84
	v_and_or_b32 v78, v79, s4, v78
	v_and_or_b32 v79, v225, s4, v84
	v_perm_b32 v84, v79, v78, s5
	v_perm_b32 v86, v79, v78, s33
	v_perm_b32 v87, v79, v78, s0
	v_perm_b32 v78, v79, v78, s1
	v_pk_fma_f16 v79, v84, s59, v81 op_sel_hi:[1,0,1]
	v_readlane_b32 s60, v120, 32
	v_alignbit_b32 v224, v76, v76, 4
	v_pk_fma_f16 v81, v86, s59, v83 op_sel_hi:[1,0,1]
	v_pk_fma_f16 v83, v87, s59, v85 op_sel_hi:[1,0,1]
	v_pk_fma_f16 v7, v78, s59, v7 op_sel_hi:[1,0,1]
	v_and_b32_e32 v78, 0x7070707, v76
	v_and_b32_e32 v84, 0x7070707, v224
	v_perm_b32 v78, s2, v205, v78
	v_perm_b32 v84, s2, v205, v84
	v_and_or_b32 v78, v76, s4, v78
	v_and_or_b32 v76, v224, s4, v84
	v_perm_b32 v85, v76, v78, s33
	v_perm_b32 v86, v76, v78, s0
	v_perm_b32 v84, v76, v78, s5
	v_perm_b32 v76, v76, v78, s1
	v_pk_fma_f16 v78, v85, s60, v80 op_sel_hi:[1,0,1]
	v_pk_fma_f16 v80, v86, s60, v82 op_sel_hi:[1,0,1]
	v_alignbit_b32 v225, v77, v77, 4
	v_pk_fma_f16 v8, v76, s60, v8 op_sel_hi:[1,0,1]
	v_and_b32_e32 v76, 0x7070707, v77
	v_and_b32_e32 v82, 0x7070707, v225
	v_pk_fma_f16 v9, v84, s60, v9 op_sel_hi:[1,0,1]
	v_perm_b32 v76, s2, v205, v76
	v_perm_b32 v82, s2, v205, v82
	v_and_or_b32 v76, v77, s4, v76
	v_and_or_b32 v77, v225, s4, v82
	v_perm_b32 v82, v77, v76, s5
	v_perm_b32 v84, v77, v76, s33
	v_perm_b32 v85, v77, v76, s0
	v_perm_b32 v76, v77, v76, s1
	v_pk_fma_f16 v77, v82, s60, v79 op_sel_hi:[1,0,1]
	v_readlane_b32 s36, v120, 36
	v_alignbit_b32 v224, v70, v70, 4
	v_pk_fma_f16 v79, v84, s60, v81 op_sel_hi:[1,0,1]
	v_pk_fma_f16 v81, v85, s60, v83 op_sel_hi:[1,0,1]
	v_pk_fma_f16 v7, v76, s60, v7 op_sel_hi:[1,0,1]
	v_and_b32_e32 v76, 0x7070707, v70
	v_and_b32_e32 v82, 0x7070707, v224
	v_perm_b32 v76, s2, v205, v76
	v_perm_b32 v82, s2, v205, v82
	v_and_or_b32 v76, v70, s4, v76
	v_and_or_b32 v70, v224, s4, v82
	v_perm_b32 v83, v70, v76, s33
	v_perm_b32 v84, v70, v76, s0
	v_perm_b32 v82, v70, v76, s5
	v_perm_b32 v70, v70, v76, s1
	v_pk_fma_f16 v76, v83, s36, v78 op_sel_hi:[1,0,1]
	v_pk_fma_f16 v78, v84, s36, v80 op_sel_hi:[1,0,1]
	v_alignbit_b32 v225, v71, v71, 4
	v_pk_fma_f16 v8, v70, s36, v8 op_sel_hi:[1,0,1]
	v_and_b32_e32 v70, 0x7070707, v71
	v_and_b32_e32 v80, 0x7070707, v225
	v_pk_fma_f16 v9, v82, s36, v9 op_sel_hi:[1,0,1]
	v_perm_b32 v70, s2, v205, v70
	v_perm_b32 v80, s2, v205, v80
	v_and_or_b32 v70, v71, s4, v70
	v_and_or_b32 v71, v225, s4, v80
	v_perm_b32 v80, v71, v70, s5
	v_perm_b32 v82, v71, v70, s33
	v_perm_b32 v83, v71, v70, s0
	v_perm_b32 v70, v71, v70, s1
	v_pk_fma_f16 v71, v80, s36, v77 op_sel_hi:[1,0,1]
	v_readlane_b32 s59, v120, 40
	v_alignbit_b32 v224, v66, v66, 4
	v_pk_fma_f16 v77, v82, s36, v79 op_sel_hi:[1,0,1]
	v_pk_fma_f16 v79, v83, s36, v81 op_sel_hi:[1,0,1]
	v_pk_fma_f16 v7, v70, s36, v7 op_sel_hi:[1,0,1]
	v_and_b32_e32 v70, 0x7070707, v66
	v_and_b32_e32 v80, 0x7070707, v224
	v_perm_b32 v70, s2, v205, v70
	v_perm_b32 v80, s2, v205, v80
	v_and_or_b32 v70, v66, s4, v70
	v_and_or_b32 v66, v224, s4, v80
	v_perm_b32 v81, v66, v70, s33
	v_perm_b32 v82, v66, v70, s0
	v_perm_b32 v80, v66, v70, s5
	v_perm_b32 v66, v66, v70, s1
	v_pk_fma_f16 v70, v81, s59, v76 op_sel_hi:[1,0,1]
	v_pk_fma_f16 v76, v82, s59, v78 op_sel_hi:[1,0,1]
	v_alignbit_b32 v225, v67, v67, 4
	v_pk_fma_f16 v8, v66, s59, v8 op_sel_hi:[1,0,1]
	v_and_b32_e32 v66, 0x7070707, v67
	v_and_b32_e32 v78, 0x7070707, v225
	v_pk_fma_f16 v9, v80, s59, v9 op_sel_hi:[1,0,1]
	v_perm_b32 v66, s2, v205, v66
	v_perm_b32 v78, s2, v205, v78
	v_and_or_b32 v66, v67, s4, v66
	v_and_or_b32 v67, v225, s4, v78
	v_perm_b32 v78, v67, v66, s5
	v_perm_b32 v80, v67, v66, s33
	v_perm_b32 v81, v67, v66, s0
	v_perm_b32 v66, v67, v66, s1
	v_pk_fma_f16 v67, v78, s59, v71 op_sel_hi:[1,0,1]
	v_readlane_b32 s60, v120, 44
	v_alignbit_b32 v224, v72, v72, 4
	v_pk_fma_f16 v71, v80, s59, v77 op_sel_hi:[1,0,1]
	v_pk_fma_f16 v77, v81, s59, v79 op_sel_hi:[1,0,1]
	v_pk_fma_f16 v7, v66, s59, v7 op_sel_hi:[1,0,1]
	v_and_b32_e32 v66, 0x7070707, v72
	v_and_b32_e32 v78, 0x7070707, v224
	v_perm_b32 v66, s2, v205, v66
	v_perm_b32 v78, s2, v205, v78
	v_and_or_b32 v66, v72, s4, v66
	v_and_or_b32 v72, v224, s4, v78
	v_perm_b32 v80, v72, v66, s0
	v_perm_b32 v78, v72, v66, s5
	v_perm_b32 v79, v72, v66, s33
	v_perm_b32 v66, v72, v66, s1
	v_pk_fma_f16 v72, v80, s60, v76 op_sel_hi:[1,0,1]
	v_alignbit_b32 v225, v73, v73, 4
	v_pk_fma_f16 v8, v66, s60, v8 op_sel_hi:[1,0,1]
	v_and_b32_e32 v66, 0x7070707, v73
	v_and_b32_e32 v76, 0x7070707, v225
	v_pk_fma_f16 v9, v78, s60, v9 op_sel_hi:[1,0,1]
	v_perm_b32 v66, s2, v205, v66
	v_perm_b32 v76, s2, v205, v76
	v_and_or_b32 v66, v73, s4, v66
	v_and_or_b32 v73, v225, s4, v76
	v_perm_b32 v76, v73, v66, s5
	v_pk_fma_f16 v70, v79, s60, v70 op_sel_hi:[1,0,1]
	v_perm_b32 v78, v73, v66, s33
	v_perm_b32 v79, v73, v66, s0
	v_perm_b32 v66, v73, v66, s1
	v_pk_fma_f16 v67, v76, s60, v67 op_sel_hi:[1,0,1]
	v_readlane_b32 s36, v120, 48
	v_alignbit_b32 v224, v68, v68, 4
	v_pk_fma_f16 v71, v78, s60, v71 op_sel_hi:[1,0,1]
	v_pk_fma_f16 v73, v79, s60, v77 op_sel_hi:[1,0,1]
	v_pk_fma_f16 v7, v66, s60, v7 op_sel_hi:[1,0,1]
	v_and_b32_e32 v66, 0x7070707, v68
	v_and_b32_e32 v76, 0x7070707, v224
	v_perm_b32 v66, s2, v205, v66
	v_perm_b32 v76, s2, v205, v76
	v_and_or_b32 v66, v68, s4, v66
	v_and_or_b32 v68, v224, s4, v76
	v_perm_b32 v77, v68, v66, s33
	v_perm_b32 v78, v68, v66, s0
	v_perm_b32 v76, v68, v66, s5
	v_perm_b32 v66, v68, v66, s1
	v_pk_fma_f16 v68, v77, s36, v70 op_sel_hi:[1,0,1]
	v_pk_fma_f16 v70, v78, s36, v72 op_sel_hi:[1,0,1]
	v_alignbit_b32 v225, v69, v69, 4
	v_pk_fma_f16 v8, v66, s36, v8 op_sel_hi:[1,0,1]
	v_and_b32_e32 v66, 0x7070707, v69
	v_and_b32_e32 v72, 0x7070707, v225
	v_pk_fma_f16 v9, v76, s36, v9 op_sel_hi:[1,0,1]
	v_perm_b32 v66, s2, v205, v66
	v_perm_b32 v72, s2, v205, v72
	v_and_or_b32 v66, v69, s4, v66
	v_and_or_b32 v69, v225, s4, v72
	v_perm_b32 v72, v69, v66, s5
	v_perm_b32 v76, v69, v66, s33
	v_perm_b32 v77, v69, v66, s0
	v_perm_b32 v66, v69, v66, s1
	v_pk_fma_f16 v67, v72, s36, v67 op_sel_hi:[1,0,1]
	v_readlane_b32 s59, v120, 52
	v_alignbit_b32 v224, v64, v64, 4
	v_pk_fma_f16 v69, v76, s36, v71 op_sel_hi:[1,0,1]
	v_pk_fma_f16 v71, v77, s36, v73 op_sel_hi:[1,0,1]
	v_pk_fma_f16 v7, v66, s36, v7 op_sel_hi:[1,0,1]
	v_and_b32_e32 v66, 0x7070707, v64
	v_and_b32_e32 v72, 0x7070707, v224
	v_perm_b32 v66, s2, v205, v66
	v_perm_b32 v72, s2, v205, v72
	v_and_or_b32 v66, v64, s4, v66
	v_and_or_b32 v64, v224, s4, v72
	v_perm_b32 v73, v64, v66, s33
	v_perm_b32 v76, v64, v66, s0
	v_perm_b32 v72, v64, v66, s5
	v_perm_b32 v64, v64, v66, s1
	v_pk_fma_f16 v66, v73, s59, v68 op_sel_hi:[1,0,1]
	v_pk_fma_f16 v68, v76, s59, v70 op_sel_hi:[1,0,1]
	v_alignbit_b32 v225, v65, v65, 4
	v_pk_fma_f16 v8, v64, s59, v8 op_sel_hi:[1,0,1]
	v_and_b32_e32 v64, 0x7070707, v65
	v_and_b32_e32 v70, 0x7070707, v225
	v_pk_fma_f16 v9, v72, s59, v9 op_sel_hi:[1,0,1]
	v_perm_b32 v64, s2, v205, v64
	v_perm_b32 v70, s2, v205, v70
	v_and_or_b32 v64, v65, s4, v64
	v_and_or_b32 v65, v225, s4, v70
	v_perm_b32 v70, v65, v64, s5
	v_perm_b32 v72, v65, v64, s33
	v_perm_b32 v73, v65, v64, s0
	v_perm_b32 v64, v65, v64, s1
	v_pk_fma_f16 v65, v70, s59, v67 op_sel_hi:[1,0,1]
	v_readlane_b32 s60, v120, 56
	v_alignbit_b32 v224, v62, v62, 4
	v_pk_fma_f16 v67, v72, s59, v69 op_sel_hi:[1,0,1]
	v_pk_fma_f16 v69, v73, s59, v71 op_sel_hi:[1,0,1]
	v_pk_fma_f16 v7, v64, s59, v7 op_sel_hi:[1,0,1]
	v_and_b32_e32 v64, 0x7070707, v62
	v_and_b32_e32 v70, 0x7070707, v224
	v_perm_b32 v64, s2, v205, v64
	v_perm_b32 v70, s2, v205, v70
	v_and_or_b32 v64, v62, s4, v64
	v_and_or_b32 v62, v224, s4, v70
	v_perm_b32 v71, v62, v64, s33
	v_perm_b32 v72, v62, v64, s0
	v_perm_b32 v70, v62, v64, s5
	v_perm_b32 v62, v62, v64, s1
	v_pk_fma_f16 v64, v71, s60, v66 op_sel_hi:[1,0,1]
	v_pk_fma_f16 v66, v72, s60, v68 op_sel_hi:[1,0,1]
	v_alignbit_b32 v225, v63, v63, 4
	v_pk_fma_f16 v8, v62, s60, v8 op_sel_hi:[1,0,1]
	v_and_b32_e32 v62, 0x7070707, v63
	v_and_b32_e32 v68, 0x7070707, v225
	v_pk_fma_f16 v9, v70, s60, v9 op_sel_hi:[1,0,1]
	v_perm_b32 v62, s2, v205, v62
	v_perm_b32 v68, s2, v205, v68
	v_and_or_b32 v62, v63, s4, v62
	v_and_or_b32 v63, v225, s4, v68
	v_perm_b32 v68, v63, v62, s5
	v_perm_b32 v70, v63, v62, s33
	v_perm_b32 v71, v63, v62, s0
	v_perm_b32 v62, v63, v62, s1
	v_pk_fma_f16 v7, v62, s60, v7 op_sel_hi:[1,0,1]
	v_readlane_b32 s36, v120, 60
	v_alignbit_b32 v224, v50, v50, 4
	v_pk_fma_f16 v63, v68, s60, v65 op_sel_hi:[1,0,1]
	v_pk_fma_f16 v65, v70, s60, v67 op_sel_hi:[1,0,1]
	v_pk_fma_f16 v67, v71, s60, v69 op_sel_hi:[1,0,1]
	v_and_b32_e32 v15, 0x7070707, v50
	v_and_b32_e32 v62, 0x7070707, v224
	v_perm_b32 v15, s2, v205, v15
	v_perm_b32 v62, s2, v205, v62
	v_and_or_b32 v15, v50, s4, v15
	v_and_or_b32 v50, v224, s4, v62
	v_perm_b32 v62, v50, v15, s5
	v_perm_b32 v68, v50, v15, s33
	v_perm_b32 v69, v50, v15, s0
	v_perm_b32 v15, v50, v15, s1
	v_pk_fma_f16 v105, v62, s36, v9 op_sel_hi:[1,0,1]
	v_alignbit_b32 v225, v51, v51, 4
	v_pk_fma_f16 v102, v15, s36, v8 op_sel_hi:[1,0,1]
	v_and_b32_e32 v8, 0x7070707, v51
	v_and_b32_e32 v9, 0x7070707, v225
	v_perm_b32 v8, s2, v205, v8
	v_perm_b32 v9, s2, v205, v9
	v_and_or_b32 v8, v51, s4, v8
	v_and_or_b32 v9, v225, s4, v9
	v_perm_b32 v15, v9, v8, s5
	v_perm_b32 v50, v9, v8, s33
	v_perm_b32 v51, v9, v8, s0
	v_perm_b32 v8, v9, v8, s1
	v_pk_fma_f16 v104, v68, s36, v64 op_sel_hi:[1,0,1]
	v_pk_fma_f16 v103, v69, s36, v66 op_sel_hi:[1,0,1]
	v_pk_fma_f16 v101, v15, s36, v63 op_sel_hi:[1,0,1]
	v_pk_fma_f16 v100, v50, s36, v65 op_sel_hi:[1,0,1]
	v_pk_fma_f16 v99, v51, s36, v67 op_sel_hi:[1,0,1]
	v_pk_fma_f16 v15, v8, s36, v7 op_sel_hi:[1,0,1]
	s_add_u32 s66, s10, s64
	s_addc_u32 s67, s11, s65
	global_load_dwordx2 v[92:93], v121, s[66:67]
	s_add_u32 s66, s12, s64
	s_addc_u32 s67, s13, s65
	global_load_dwordx2 v[90:91], v121, s[66:67]
	s_add_u32 s66, s14, s64
	s_addc_u32 s67, s15, s65
	global_load_dwordx2 v[88:89], v121, s[66:67]
	s_add_u32 s66, s16, s64
	s_addc_u32 s67, s17, s65
	global_load_dwordx2 v[86:87], v121, s[66:67]
	s_add_u32 s66, s18, s64
	s_addc_u32 s67, s19, s65
	global_load_dwordx2 v[84:85], v121, s[66:67]
	s_add_u32 s66, s20, s64
	s_addc_u32 s67, s21, s65
	global_load_dwordx2 v[82:83], v121, s[66:67]
	s_add_u32 s66, s22, s64
	s_addc_u32 s67, s23, s65
	global_load_dwordx2 v[80:81], v121, s[66:67]
	s_add_u32 s66, s24, s64
	s_addc_u32 s67, s25, s65
	global_load_dwordx2 v[78:79], v121, s[66:67]
	s_add_u32 s66, s26, s64
	s_addc_u32 s67, s27, s65
	global_load_dwordx2 v[76:77], v121, s[66:67]
	s_add_u32 s66, s28, s64
	s_addc_u32 s67, s29, s65
	global_load_dwordx2 v[70:71], v121, s[66:67]
	s_add_u32 s66, s30, s64
	s_addc_u32 s67, s31, s65
	global_load_dwordx2 v[66:67], v121, s[66:67]
	s_add_u32 s66, s34, s64
	s_addc_u32 s67, s35, s65
	global_load_dwordx2 v[72:73], v121, s[66:67]
	s_add_u32 s66, s38, s64
	s_addc_u32 s67, s39, s65
	global_load_dwordx2 v[68:69], v121, s[66:67]
	s_add_u32 s66, s50, s64
	s_addc_u32 s67, s51, s65
	global_load_dwordx2 v[64:65], v121, s[66:67]
	s_add_u32 s66, s52, s64
	s_addc_u32 s67, s53, s65
	global_load_dwordx2 v[62:63], v121, s[66:67]
	s_add_u32 s66, s54, s64
	s_addc_u32 s67, s55, s65
	global_load_dwordx2 v[50:51], v121, s[66:67]
	s_cmpk_eq_i32 s56, 0x90
	s_cbranch_scc0 .LBB0_770
	v_lshl_add_u64 v[94:95], v[2:3], 2, v[44:45]
	v_mov_b32_e32 v106, v208
	v_mov_b32_e32 v107, v209
	v_mov_b32_e32 v108, v210
	v_mov_b32_e32 v109, v211
	v_mov_b32_e32 v8, v212
	v_mov_b32_e32 v9, v213
	v_mov_b32_e32 v10, v214
	v_mov_b32_e32 v11, v215
	v_mov_b32_e32 v4, v216
	v_mov_b32_e32 v5, v217
	v_mov_b32_e32 v6, v218
	v_mov_b32_e32 v7, v219
	v_mov_b32_e32 v0, v220
	v_mov_b32_e32 v1, v221
	v_mov_b32_e32 v2, v222
	v_mov_b32_e32 v3, v223
	v_cvt_f32_f16_sdwa v13, v105 dst_sel:DWORD dst_unused:UNUSED_PAD src0_sel:WORD_1
	v_cvt_f32_f16_e32 v12, v105
	s_mov_b32 s12, 0x800000
	v_readlane_b32 s10, v255, 5
	v_readlane_b32 s11, v255, 6
	v_pk_add_f32 v[0:1], v[0:1], v[12:13]
	v_cvt_f32_f16_sdwa v13, v104 dst_sel:DWORD dst_unused:UNUSED_PAD src0_sel:WORD_1
	v_cvt_f32_f16_e32 v12, v104
	v_lshl_add_u64 v[48:49], v[48:49], 0, s[10:11]
	v_pk_add_f32 v[2:3], v[2:3], v[12:13]
	v_cvt_f32_f16_sdwa v13, v103 dst_sel:DWORD dst_unused:UNUSED_PAD src0_sel:WORD_1
	v_cvt_f32_f16_e32 v12, v103
	global_store_dwordx4 v[94:95], v[0:3], off
	v_pk_add_f32 v[4:5], v[4:5], v[12:13]
	v_cvt_f32_f16_sdwa v13, v102 dst_sel:DWORD dst_unused:UNUSED_PAD src0_sel:WORD_1
	v_cvt_f32_f16_e32 v12, v102
	v_mov_b32_e32 v102, v1
	v_mov_b32_e32 v103, v5
	v_pk_mul_f32 v[102:103], v[102:103], v[102:103]
	v_pk_add_f32 v[6:7], v[6:7], v[12:13]
	v_mov_b32_e32 v12, v0
	v_mov_b32_e32 v13, v4
	v_pk_fma_f32 v[12:13], v[12:13], v[12:13], v[102:103]
	v_mov_b32_e32 v102, v2
	v_mov_b32_e32 v103, v6
	v_pk_fma_f32 v[12:13], v[102:103], v[102:103], v[12:13]
	v_mov_b32_e32 v102, v3
	v_mov_b32_e32 v103, v7
	v_pk_fma_f32 v[102:103], v[102:103], v[102:103], v[12:13]
	v_cvt_f32_f16_sdwa v13, v101 dst_sel:DWORD dst_unused:UNUSED_PAD src0_sel:WORD_1
	v_cvt_f32_f16_e32 v12, v101
	v_cvt_f32_f16_sdwa v101, v15 dst_sel:DWORD dst_unused:UNUSED_PAD src0_sel:WORD_1
	global_store_dwordx4 v[94:95], v[4:7], off offset:16
	v_pk_add_f32 v[8:9], v[8:9], v[12:13]
	v_cvt_f32_f16_sdwa v13, v100 dst_sel:DWORD dst_unused:UNUSED_PAD src0_sel:WORD_1
	v_cvt_f32_f16_e32 v12, v100
	v_cvt_f32_f16_e32 v100, v15
	v_pk_add_f32 v[10:11], v[10:11], v[12:13]
	v_cvt_f32_f16_sdwa v13, v99 dst_sel:DWORD dst_unused:UNUSED_PAD src0_sel:WORD_1
	v_cvt_f32_f16_e32 v12, v99
	v_pk_add_f32 v[14:15], v[108:109], v[100:101]
	v_mov_b32_e32 v100, v9
	global_store_dwordx4 v[94:95], v[8:11], off offset:32
	v_pk_add_f32 v[12:13], v[106:107], v[12:13]
	global_store_dwordx4 v[94:95], v[12:15], off offset:48
	v_mov_b32_e32 v101, v13
	v_mov_b32_e32 v94, v8
	v_mov_b32_e32 v95, v12
	v_pk_mul_f32 v[100:101], v[100:101], v[100:101]
	v_add_f32_e32 v99, v102, v103
	v_pk_fma_f32 v[94:95], v[94:95], v[94:95], v[100:101]
	v_mov_b32_e32 v100, v10
	v_mov_b32_e32 v101, v14
	v_pk_fma_f32 v[94:95], v[100:101], v[100:101], v[94:95]
	v_mov_b32_e32 v100, v11
	v_mov_b32_e32 v101, v15
	v_pk_fma_f32 v[94:95], v[100:101], v[100:101], v[94:95]
	global_load_dwordx4 v[100:103], v[46:47], off offset:48
	global_load_dwordx4 v[104:107], v[46:47], off offset:32
	global_load_dwordx4 v[108:111], v[46:47], off offset:16
	global_load_dwordx4 v[112:115], v[46:47], off
	v_add_f32_e32 v94, v99, v94
	v_add_f32_e32 v94, v94, v95
	v_mov_b32_e32 v95, v94
	s_nop 1
	v_permlane32_swap_b32 v95, v94
	s_waitcnt lgkmcnt(0)
	v_add_f32_e32 v94, v94, v95
	v_mov_b32_e32 v95, v94
	s_nop 1
	v_permlane16_swap_b32 v95, v94
	s_waitcnt lgkmcnt(0)
	v_add_f32_e32 v94, v94, v95
	s_nop 1
	v_mov_b32_dpp v95, v94 row_ror:8 row_mask:0xf bank_mask:0xf
	s_waitcnt lgkmcnt(0)
	v_add_f32_e32 v94, v94, v95
	s_nop 1
	v_mov_b32_dpp v95, v94 row_half_mirror row_mask:0xf bank_mask:0xf
	s_nop 1
	v_mov_b32_dpp v95, v95 quad_perm:[3,2,1,0] row_mask:0xf bank_mask:0xf
	s_waitcnt lgkmcnt(0)
	v_add_f32_e32 v94, v94, v95
	s_nop 1
	v_mov_b32_dpp v95, v94 quad_perm:[2,3,0,1] row_mask:0xf bank_mask:0xf
	s_waitcnt lgkmcnt(0)
	v_add_f32_e32 v94, v94, v95
	s_nop 1
	v_mov_b32_dpp v95, v94 quad_perm:[1,0,3,2] row_mask:0xf bank_mask:0xf
	s_waitcnt lgkmcnt(0)
	v_add_f32_e32 v94, v94, v95
	v_fmamk_f32 v94, v94, 0x3a800000, v191
	v_cmp_gt_f32_e32 vcc, s12, v94
	v_mul_f32_e32 v95, 0x4b800000, v94
	s_nop 0
	v_cndmask_b32_e32 v94, v94, v95, vcc
	v_rsq_f32_e32 v94, v94
	s_nop 0
	v_mul_f32_e32 v95, 0x45800000, v94
	v_cndmask_b32_e32 v94, v94, v95, vcc
	v_pk_mul_f32 v[0:1], v[0:1], v[94:95] op_sel_hi:[1,0]
	v_pk_mul_f32 v[2:3], v[2:3], v[94:95] op_sel_hi:[1,0]
	s_waitcnt vmcnt(0)
	v_pk_mul_f32 v[0:1], v[112:113], v[0:1]
	v_pk_mul_f32 v[2:3], v[114:115], v[2:3]
	v_cvt_pk_bf16_f32 v0, v0, v1
	v_cvt_pk_bf16_f32 v1, v2, v3
	v_pk_mul_f32 v[2:3], v[4:5], v[94:95] op_sel_hi:[1,0]
	v_pk_mul_f32 v[4:5], v[6:7], v[94:95] op_sel_hi:[1,0]
	v_pk_mul_f32 v[2:3], v[108:109], v[2:3]
	v_pk_mul_f32 v[4:5], v[110:111], v[4:5]
	v_cvt_pk_bf16_f32 v2, v2, v3
	v_cvt_pk_bf16_f32 v3, v4, v5
	v_pk_mul_f32 v[4:5], v[8:9], v[94:95] op_sel_hi:[1,0]
	v_pk_mul_f32 v[6:7], v[10:11], v[94:95] op_sel_hi:[1,0]
	v_pk_mul_f32 v[4:5], v[104:105], v[4:5]
	v_pk_mul_f32 v[6:7], v[6:7], v[106:107]
	v_cvt_pk_bf16_f32 v4, v4, v5
	v_cvt_pk_bf16_f32 v5, v6, v7
	v_pk_mul_f32 v[6:7], v[12:13], v[94:95] op_sel_hi:[1,0]
	v_pk_mul_f32 v[8:9], v[14:15], v[94:95] op_sel_hi:[1,0]
	v_pk_mul_f32 v[6:7], v[6:7], v[100:101]
	v_pk_mul_f32 v[8:9], v[8:9], v[102:103]
	v_cvt_pk_bf16_f32 v6, v6, v7
	v_cvt_pk_bf16_f32 v7, v8, v9
	global_store_dwordx4 v[74:75], v[0:3], off
	global_store_dwordx4 v[74:75], v[4:7], off offset:16
	s_nop 0
	v_mov_b32_e32 v0, v98
	s_andn2_b64 exec, exec, s[8:9]
	s_cbranch_execnz .LBB0_769
